# attention latent loop: second LDS write of each staged K/V pair reuses the first address (+8192 immediate); unit-invariant part of the prefetch bases hoisted out of the tile loop
# speedup vs baseline: 1.0115x; 1.0036x over previous
.LBB0_786:
	v_and_b32_e32 v34, 63, v171
	s_lshl_b32 s16, s0, 8
	v_and_b32_e32 v35, 0x3fffffc0, v172
	v_readlane_b32 s0, v254, 42
	v_lshlrev_b32_e32 v36, 4, v34
	v_and_b32_e32 v36, 0xc0, v36
	v_lshl_add_u32 v177, v35, 2, s0
	v_lshlrev_b32_e32 v35, 3, v34
	v_lshlrev_b32_e32 v37, 1, v34
	v_and_or_b32 v36, v35, 24, v36
	v_and_b32_e32 v37, 32, v37
	v_and_b32_e32 v35, 0x100, v35
	v_or3_b32 v192, v36, v37, v35
	s_add_i32 s1, 0, 0x400
	v_add_u32_e32 v194, s1, v192
	s_add_i32 s1, 0, 0x10400
	s_waitcnt vmcnt(4)
	s_waitcnt vmcnt(7)
	ds_write_b128 v32, v[16:19] offset:17408
	s_waitcnt vmcnt(6)
	ds_write_b128 v33, v[20:23] offset:17408
	v_add_u32_e32 v16, s1, v182
	v_exp_f32_e32 v159, v0
	v_exp_f32_e32 v161, v1
	v_exp_f32_e32 v157, v2
	v_exp_f32_e32 v160, v3
	v_exp_f32_e32 v155, v4
	v_exp_f32_e32 v158, v5
	v_exp_f32_e32 v154, v6
	v_exp_f32_e32 v156, v7
	v_exp_f32_e32 v151, v8
	v_exp_f32_e32 v153, v9
	v_exp_f32_e32 v149, v10
	v_exp_f32_e32 v152, v11
	v_exp_f32_e32 v147, v12
	v_exp_f32_e32 v150, v13
	v_exp_f32_e32 v146, v14
	v_exp_f32_e32 v148, v15
	s_waitcnt vmcnt(5)
	ds_write_b128 v16, v[24:27]
	v_add_u32_e32 v16, s1, v183
	v_mov_b32_e32 v14, v113
	v_mov_b32_e32 v15, v113
	s_waitcnt vmcnt(4)
	ds_write_b128 v16, v[28:31]
	v_cmp_gt_u32_e64 s[38:39], 32, v34
	v_mov_b32_e32 v0, v113
	v_mov_b32_e32 v1, v113
	v_mov_b32_e32 v2, v113
	v_mov_b32_e32 v3, v113
	v_mov_b32_e32 v4, v113
	v_mov_b32_e32 v5, v113
	v_mov_b32_e32 v6, v113
	v_mov_b32_e32 v7, v113
	v_mov_b32_e32 v8, v113
	v_mov_b32_e32 v9, v113
	v_mov_b32_e32 v10, v113
	v_mov_b32_e32 v11, v113
	v_mov_b32_e32 v12, v113
	v_mov_b32_e32 v13, v113
	v_mov_b64_e32 v[62:63], v[14:15]
	v_mov_b64_e32 v[46:47], v[14:15]
	v_mov_b64_e32 v[30:31], v[14:15]
	s_add_i32 s16, s16, 0x8000
	s_mov_b32 s19, 2
	s_mov_b32 s28, 4
	s_mov_b32 s0, 1
	v_lshl_add_u32 v178, v173, 2, v177
	s_mov_b32 s29, 0
	v_mov_b32_e32 v179, 0
	v_mov_b64_e32 v[60:61], v[12:13]
	v_mov_b64_e32 v[58:59], v[10:11]
	v_mov_b64_e32 v[56:57], v[8:9]
	v_mov_b64_e32 v[54:55], v[6:7]
	v_mov_b64_e32 v[52:53], v[4:5]
	v_mov_b64_e32 v[50:51], v[2:3]
	v_mov_b64_e32 v[48:49], v[0:1]
	v_mov_b64_e32 v[44:45], v[12:13]
	v_mov_b64_e32 v[42:43], v[10:11]
	v_mov_b64_e32 v[40:41], v[8:9]
	v_mov_b64_e32 v[38:39], v[6:7]
	v_mov_b64_e32 v[36:37], v[4:5]
	v_mov_b64_e32 v[34:35], v[2:3]
	v_mov_b64_e32 v[32:33], v[0:1]
	v_mov_b64_e32 v[28:29], v[12:13]
	v_mov_b64_e32 v[26:27], v[10:11]
	v_mov_b64_e32 v[24:25], v[8:9]
	v_mov_b64_e32 v[22:23], v[6:7]
	v_mov_b64_e32 v[20:21], v[4:5]
	v_mov_b64_e32 v[18:19], v[2:3]
	v_mov_b64_e32 v[16:17], v[0:1]
	s_waitcnt lgkmcnt(0)
	s_add_u32 s78, s8, s96
	s_addc_u32 s79, s9, 0
	s_add_u32 s80, s6, s96
	s_addc_u32 s81, s7, 0
	s_barrier
.LBB0_787:
	s_mov_b32 s54, s0
	s_add_i32 s55, s28, -3
	s_lshl_b32 s21, s0, 14
	v_add_u32_e32 v180, s21, v191
	v_add_u32_e32 v84, v180, v190
	ds_read_b128 v[80:83], v84 offset:50176
	ds_read_b128 v[84:87], v84 offset:58368
	v_add_u32_e32 v195, v180, v188
	ds_read_b128 v[196:199], v195 offset:50176
	ds_read_b128 v[200:203], v195 offset:58368
	v_add_u32_e32 v195, v180, v187
	s_waitcnt lgkmcnt(3)
	v_mfma_f32_32x32x16_bf16 v[96:111], v[80:83], v[122:125], 0
	v_add_u32_e32 v180, v180, v186
	v_exp_f32_e32 v204, v72
	v_exp_f32_e32 v205, v73
	v_exp_f32_e32 v206, v74
	v_exp_f32_e32 v207, v75
	v_exp_f32_e32 v208, v76
	v_exp_f32_e32 v209, v77
	s_waitcnt lgkmcnt(2)
	v_mfma_f32_32x32x16_bf16 v[80:95], v[84:87], v[122:125], 0
	v_exp_f32_e32 v210, v78
	v_exp_f32_e32 v79, v79
	s_waitcnt lgkmcnt(1)
	v_mfma_f32_32x32x16_bf16 v[96:111], v[196:199], v[126:129], v[96:111]
	s_waitcnt lgkmcnt(0)
	v_mfma_f32_32x32x16_bf16 v[80:95], v[200:203], v[126:129], v[80:95]
	ds_read_b128 v[196:199], v195 offset:50176
	ds_read_b128 v[200:203], v195 offset:58368
	s_waitcnt lgkmcnt(1)
	v_mfma_f32_32x32x16_bf16 v[96:111], v[196:199], v[118:121], v[96:111]
	s_waitcnt lgkmcnt(0)
	v_mfma_f32_32x32x16_bf16 v[80:95], v[200:203], v[118:121], v[80:95]
	ds_read_b128 v[196:199], v180 offset:50176
	ds_read_b128 v[200:203], v180 offset:58368
	v_exp_f32_e32 v180, v64
	v_add_f32_e32 v64, v161, v159
	v_add_f32_e32 v195, v157, v160
	v_add_f32_e32 v64, v155, v64
	v_add_f32_e32 v195, v158, v195
	v_add_f32_e32 v64, v154, v64
	v_add_f32_e32 v195, v156, v195
	v_add_f32_e32 v64, v151, v64
	v_add_f32_e32 v195, v153, v195
	v_add_f32_e32 v64, v149, v64
	v_add_f32_e32 v195, v152, v195
	v_add_f32_e32 v64, v147, v64
	s_waitcnt lgkmcnt(1)
	v_mfma_f32_32x32x16_bf16 v[96:111], v[196:199], v[114:117], v[96:111]
	v_exp_f32_e32 v197, v65
	v_add_f32_e32 v195, v150, v195
	v_exp_f32_e32 v198, v66
	v_add_f32_e32 v64, v146, v64
	v_exp_f32_e32 v199, v67
	v_add_f32_e32 v195, v148, v195
	v_add_f32_e32 v64, v180, v64
	s_waitcnt lgkmcnt(0)
	v_mfma_f32_32x32x16_bf16 v[80:95], v[200:203], v[114:117], v[80:95]
	v_exp_f32_e32 v200, v68
	v_exp_f32_e32 v201, v69
	v_add_f32_e32 v195, v197, v195
	v_exp_f32_e32 v202, v70
	v_add_f32_e32 v64, v198, v64
	v_exp_f32_e32 v203, v71
	v_add_f32_e32 v195, v199, v195
	v_add_f32_e32 v64, v200, v64
	v_add_f32_e32 v195, v201, v195
	v_add_f32_e32 v64, v202, v64
	v_add_f32_e32 v195, v203, v195
	v_add_f32_e32 v64, v204, v64
	v_add_f32_e32 v195, v205, v195
	v_add_f32_e32 v64, v206, v64
	v_add_f32_e32 v195, v207, v195
	v_add_f32_e32 v64, v208, v64
	v_add_f32_e32 v195, v209, v195
	v_add_f32_e32 v64, v210, v64
	v_add_f32_e32 v195, v79, v195
	v_add_f32_e32 v195, v195, v64
	v_cvt_pk_bf16_f32 v64, v159, v161
	v_cvt_pk_bf16_f32 v65, v157, v160
	v_cvt_pk_bf16_f32 v66, v155, v158
	v_cvt_pk_bf16_f32 v67, v154, v156
	v_cvt_pk_bf16_f32 v68, v151, v153
	v_cvt_pk_bf16_f32 v69, v149, v152
	v_cvt_pk_bf16_f32 v70, v147, v150
	v_cvt_pk_bf16_f32 v71, v146, v148
	v_cvt_pk_bf16_f32 v72, v180, v197
	v_cvt_pk_bf16_f32 v73, v198, v199
	v_cvt_pk_bf16_f32 v74, v200, v201
	v_cvt_pk_bf16_f32 v75, v202, v203
	v_cvt_pk_bf16_f32 v76, v204, v205
	v_cvt_pk_bf16_f32 v77, v206, v207
	v_cvt_pk_bf16_f32 v78, v208, v209
	v_cvt_pk_bf16_f32 v79, v210, v79
	s_cmp_lt_u32 s55, 30
	s_cselect_b32 s0, 0, 0xffffffe0
	s_cselect_b32 s1, s18, s16
	s_add_i32 s0, s0, s28
	s_lshl_b32 s0, s0, 6
	s_add_i32 s0, s0, s1
	s_sub_i32 s0, s0, 64
	s_mul_i32 s64, s0, 0x1800
	s_add_u32 s66, s78, s64
	s_addc_u32 s67, s79, 0
	s_add_u32 s68, s66, 0x30000
	s_addc_u32 s69, s67, 0
	s_add_u32 s70, s80, s64
	s_addc_u32 s71, s81, 0
	s_add_u32 s72, s70, 0x30000
	s_addc_u32 s73, s71, 0
	global_load_dwordx4 v[146:149], v241, s[66:67]
	global_load_dwordx4 v[150:153], v241, s[68:69]
	global_load_dwordx4 v[154:157], v241, s[70:71]
	global_load_dwordx4 v[158:161], v241, s[72:73]
	s_lshl_b32 s20, s29, 14
	v_add_u32_e32 v180, s20, v194
	ds_read_b64_tr_b16 v[198:199], v180 offset:0
	ds_read_b64_tr_b16 v[200:201], v180 offset:0x800
	ds_read_b64_tr_b16 v[202:203], v180 offset:0x1000
	ds_read_b64_tr_b16 v[204:205], v180 offset:0x1800
	ds_read_b64_tr_b16 v[206:207], v180 offset:0x2000
	ds_read_b64_tr_b16 v[208:209], v180 offset:0x2800
	ds_read_b64_tr_b16 v[222:223], v180 offset:0x3000
	ds_read_b64_tr_b16 v[224:225], v180 offset:0x3800
	s_waitcnt lgkmcnt(0)
	s_nop 0
	v_mfma_f32_32x32x16_bf16 v[0:15], v[64:67], v[198:201], v[0:15]
	ds_read_b64_tr_b16 v[198:199], v180 offset:0x200
	ds_read_b64_tr_b16 v[200:201], v180 offset:0xa00
	v_mfma_f32_32x32x16_bf16 v[0:15], v[68:71], v[202:205], v[0:15]
	ds_read_b64_tr_b16 v[202:203], v180 offset:0x1200
	ds_read_b64_tr_b16 v[204:205], v180 offset:0x1a00
	v_mfma_f32_32x32x16_bf16 v[0:15], v[72:75], v[206:209], v[0:15]
	ds_read_b64_tr_b16 v[206:207], v180 offset:0x2200
	ds_read_b64_tr_b16 v[208:209], v180 offset:0x2a00
	v_mfma_f32_32x32x16_bf16 v[0:15], v[76:79], v[222:225], v[0:15]
	ds_read_b64_tr_b16 v[222:223], v180 offset:0x3200
	ds_read_b64_tr_b16 v[224:225], v180 offset:0x3a00
	s_waitcnt lgkmcnt(0)
	v_mfma_f32_32x32x16_bf16 v[48:63], v[64:67], v[198:201], v[48:63]
	ds_read_b64_tr_b16 v[198:199], v180 offset:0x400
	ds_read_b64_tr_b16 v[200:201], v180 offset:0xc00
	v_mfma_f32_32x32x16_bf16 v[48:63], v[68:71], v[202:205], v[48:63]
	ds_read_b64_tr_b16 v[202:203], v180 offset:0x1400
	ds_read_b64_tr_b16 v[204:205], v180 offset:0x1c00
	v_mfma_f32_32x32x16_bf16 v[48:63], v[72:75], v[206:209], v[48:63]
	ds_read_b64_tr_b16 v[206:207], v180 offset:0x2400
	ds_read_b64_tr_b16 v[208:209], v180 offset:0x2c00
	v_mfma_f32_32x32x16_bf16 v[48:63], v[76:79], v[222:225], v[48:63]
	ds_read_b64_tr_b16 v[222:223], v180 offset:0x3400
	ds_read_b64_tr_b16 v[224:225], v180 offset:0x3c00
	s_waitcnt lgkmcnt(0)
	v_mfma_f32_32x32x16_bf16 v[32:47], v[64:67], v[198:201], v[32:47]
	ds_read_b64_tr_b16 v[198:199], v180 offset:0x600
	ds_read_b64_tr_b16 v[200:201], v180 offset:0xe00
	v_mfma_f32_32x32x16_bf16 v[32:47], v[68:71], v[202:205], v[32:47]
	ds_read_b64_tr_b16 v[202:203], v180 offset:0x1600
	ds_read_b64_tr_b16 v[204:205], v180 offset:0x1e00
	v_mfma_f32_32x32x16_bf16 v[32:47], v[72:75], v[206:209], v[32:47]
	ds_read_b64_tr_b16 v[206:207], v180 offset:0x2600
	ds_read_b64_tr_b16 v[208:209], v180 offset:0x2e00
	v_mfma_f32_32x32x16_bf16 v[32:47], v[76:79], v[222:225], v[32:47]
	ds_read_b64_tr_b16 v[222:223], v180 offset:0x3600
	ds_read_b64_tr_b16 v[224:225], v180 offset:0x3e00
	s_waitcnt lgkmcnt(0)
	v_mfma_f32_32x32x16_bf16 v[16:31], v[64:67], v[198:201], v[16:31]
	v_max_f32_e32 v64, v96, v97
	v_max3_f32 v65, v80, v81, v82
	v_max3_f32 v64, v64, v98, v99
	v_max3_f32 v65, v65, v83, v84
	v_max3_f32 v64, v64, v100, v101
	v_mfma_f32_32x32x16_bf16 v[16:31], v[68:71], v[202:205], v[16:31]
	v_max3_f32 v65, v65, v85, v86
	v_max3_f32 v64, v64, v102, v103
	v_max3_f32 v65, v65, v87, v88
	v_max3_f32 v64, v64, v104, v105
	v_max3_f32 v65, v65, v89, v90
	v_max3_f32 v64, v64, v106, v107
	v_max3_f32 v65, v65, v91, v92
	v_mfma_f32_32x32x16_bf16 v[16:31], v[72:75], v[206:209], v[16:31]
	v_max3_f32 v64, v64, v108, v109
	v_max3_f32 v65, v65, v93, v94
	v_max3_f32 v64, v64, v110, v111
	v_max3_f32 v64, v64, v65, v95
	v_mov_b32_e32 v198, 1.0
	v_mfma_f32_32x32x16_bf16 v[16:31], v[76:79], v[222:225], v[16:31]
	v_cmp_ge_f32_e64 s[40:41], s75, v64
	s_and_b64 s[0:1], s[56:57], s[40:41]
	s_cmp_eq_u64 s[0:1], exec
	s_cbranch_scc0 .LBB0_801
.LBB0_788:
	s_lshl_b32 s0, s19, 14
	s_add_i32 s22, s0, 0
	v_add_u32_e32 v64, s22, v184
	s_waitcnt vmcnt(4)
	s_waitcnt vmcnt(4)
	ds_write_b128 v64, v[130:133] offset:1024
	ds_write_b128 v64, v[134:137] offset:9216
	v_add_u32_e32 v64, s22, v182
	ds_write_b128 v64, v[138:141] offset:50176
	v_cmp_gt_f32_e32 vcc, 1.0, v198
	ds_write_b128 v64, v[142:145] offset:58368
	s_cbranch_vccz .LBB0_792
	s_and_saveexec_b64 s[0:1], s[38:39]
	ds_write_b32 v178, v198 offset:128
	s_or_b64 exec, exec, s[0:1]
	s_waitcnt lgkmcnt(0)
	v_add_u32_e32 v76, v177, v112
	ds_read_b128 v[64:67], v76 offset:224
	ds_read_b128 v[68:71], v76 offset:192
	ds_read_b128 v[72:75], v76 offset:160
	ds_read_b128 v[76:79], v76 offset:128
	s_waitcnt lgkmcnt(3)
	v_pk_mul_f32 v[12:13], v[12:13], v[64:65]
	s_waitcnt lgkmcnt(2)
	v_pk_mul_f32 v[8:9], v[8:9], v[68:69]
	s_waitcnt lgkmcnt(1)
	v_pk_mul_f32 v[4:5], v[4:5], v[72:73]
	v_pk_mul_f32 v[14:15], v[14:15], v[66:67]
	v_pk_mul_f32 v[10:11], v[10:11], v[70:71]
	v_pk_mul_f32 v[6:7], v[6:7], v[74:75]
	s_waitcnt lgkmcnt(0)
	v_pk_mul_f32 v[2:3], v[2:3], v[78:79]
	v_pk_mul_f32 v[0:1], v[0:1], v[76:77]
	v_pk_mul_f32 v[60:61], v[60:61], v[64:65]
	v_pk_mul_f32 v[56:57], v[56:57], v[68:69]
	v_pk_mul_f32 v[52:53], v[52:53], v[72:73]
	v_pk_mul_f32 v[62:63], v[62:63], v[66:67]
	v_pk_mul_f32 v[58:59], v[58:59], v[70:71]
	v_pk_mul_f32 v[54:55], v[54:55], v[74:75]
	v_pk_mul_f32 v[50:51], v[50:51], v[78:79]
	v_pk_mul_f32 v[48:49], v[48:49], v[76:77]
	v_pk_mul_f32 v[44:45], v[44:45], v[64:65]
	v_pk_mul_f32 v[40:41], v[40:41], v[68:69]
	v_pk_mul_f32 v[36:37], v[36:37], v[72:73]
	v_pk_mul_f32 v[46:47], v[46:47], v[66:67]
	v_pk_mul_f32 v[42:43], v[42:43], v[70:71]
	v_pk_mul_f32 v[38:39], v[38:39], v[74:75]
	v_pk_mul_f32 v[34:35], v[34:35], v[78:79]
	v_pk_mul_f32 v[32:33], v[32:33], v[76:77]
	v_pk_mul_f32 v[28:29], v[28:29], v[64:65]
	v_pk_mul_f32 v[24:25], v[24:25], v[68:69]
	v_pk_mul_f32 v[20:21], v[20:21], v[72:73]
	v_pk_mul_f32 v[30:31], v[30:31], v[66:67]
	v_pk_mul_f32 v[26:27], v[26:27], v[70:71]
	v_pk_mul_f32 v[22:23], v[22:23], v[74:75]
	v_pk_mul_f32 v[18:19], v[18:19], v[78:79]
	v_pk_mul_f32 v[16:17], v[16:17], v[76:77]
.LBB0_792:
	v_exp_f32_e32 v197, v96
	v_exp_f32_e32 v208, v97
	v_exp_f32_e32 v209, v98
	v_exp_f32_e32 v210, v99
	v_exp_f32_e32 v211, v100
	v_exp_f32_e32 v220, v101
	v_exp_f32_e32 v221, v102
	v_exp_f32_e32 v222, v103
	v_exp_f32_e32 v223, v104
	v_exp_f32_e32 v224, v105
	v_exp_f32_e32 v225, v106
	v_exp_f32_e32 v226, v107
	v_exp_f32_e32 v227, v108
	v_exp_f32_e32 v228, v109
	v_exp_f32_e32 v229, v110
	v_exp_f32_e32 v230, v111
	s_waitcnt lgkmcnt(0)
	s_barrier
	v_add_u32_e32 v199, s22, v189
	v_add_u32_e32 v68, v199, v190
	ds_read_b128 v[64:67], v68 offset:50176
	ds_read_b128 v[68:71], v68 offset:58368
	v_add_u32_e32 v204, v199, v188
	ds_read_b128 v[200:203], v204 offset:50176
	ds_read_b128 v[204:207], v204 offset:58368
	v_exp_f32_e32 v231, v87
	s_waitcnt lgkmcnt(3)
	v_mfma_f32_32x32x16_bf16 v[96:111], v[64:67], v[122:125], 0
	v_exp_f32_e32 v232, v88
	v_exp_f32_e32 v233, v89
	v_exp_f32_e32 v234, v90
	v_exp_f32_e32 v235, v91
	v_exp_f32_e32 v236, v92
	v_exp_f32_e32 v237, v93
	v_exp_f32_e32 v238, v94
	s_waitcnt lgkmcnt(2)
	v_mfma_f32_32x32x16_bf16 v[64:79], v[68:71], v[122:125], 0
	v_exp_f32_e32 v95, v95
	s_waitcnt lgkmcnt(1)
	v_mfma_f32_32x32x16_bf16 v[96:111], v[200:203], v[126:129], v[96:111]
	s_waitcnt lgkmcnt(0)
	v_mfma_f32_32x32x16_bf16 v[64:79], v[204:207], v[126:129], v[64:79]
	v_add_u32_e32 v204, v199, v187
	ds_read_b128 v[200:203], v204 offset:50176
	ds_read_b128 v[204:207], v204 offset:58368
	v_add_u32_e32 v199, v199, v186
	s_waitcnt lgkmcnt(1)
	v_mfma_f32_32x32x16_bf16 v[96:111], v[200:203], v[118:121], v[96:111]
	s_waitcnt lgkmcnt(0)
	v_mfma_f32_32x32x16_bf16 v[64:79], v[204:207], v[118:121], v[64:79]
	ds_read_b128 v[200:203], v199 offset:50176
	ds_read_b128 v[204:207], v199 offset:58368
	s_waitcnt lgkmcnt(1)
	v_mfma_f32_32x32x16_bf16 v[96:111], v[200:203], v[114:117], v[96:111]
	v_exp_f32_e32 v201, v80
	v_add_f32_e32 v80, v208, v197
	v_add_f32_e32 v199, v209, v210
	v_add_f32_e32 v80, v211, v80
	v_add_f32_e32 v199, v220, v199
	v_add_f32_e32 v80, v221, v80
	v_add_f32_e32 v199, v222, v199
	v_add_f32_e32 v80, v223, v80
	v_add_f32_e32 v199, v224, v199
	v_add_f32_e32 v80, v225, v80
	v_add_f32_e32 v199, v226, v199
	v_add_f32_e32 v80, v227, v80
	v_exp_f32_e32 v202, v81
	v_add_f32_e32 v199, v228, v199
	v_exp_f32_e32 v203, v82
	v_add_f32_e32 v80, v229, v80
	s_waitcnt lgkmcnt(0)
	v_mfma_f32_32x32x16_bf16 v[64:79], v[204:207], v[114:117], v[64:79]
	v_exp_f32_e32 v204, v83
	v_add_f32_e32 v199, v230, v199
	v_exp_f32_e32 v205, v84
	v_add_f32_e32 v80, v201, v80
	v_exp_f32_e32 v206, v85
	v_add_f32_e32 v199, v202, v199
	v_exp_f32_e32 v207, v86
	v_add_f32_e32 v80, v203, v80
	v_add_f32_e32 v199, v204, v199
	v_add_f32_e32 v80, v205, v80
	v_add_f32_e32 v199, v206, v199
	v_add_f32_e32 v80, v207, v80
	v_add_f32_e32 v199, v231, v199
	v_add_f32_e32 v80, v232, v80
	v_add_f32_e32 v199, v233, v199
	v_add_f32_e32 v80, v234, v80
	v_add_f32_e32 v199, v235, v199
	v_add_f32_e32 v80, v236, v80
	v_add_f32_e32 v199, v237, v199
	v_add_f32_e32 v80, v238, v80
	v_add_f32_e32 v199, v95, v199
	v_add_f32_e32 v199, v199, v80
	v_cvt_pk_bf16_f32 v80, v197, v208
	v_cvt_pk_bf16_f32 v81, v209, v210
	v_cvt_pk_bf16_f32 v82, v211, v220
	v_cvt_pk_bf16_f32 v83, v221, v222
	v_cvt_pk_bf16_f32 v84, v223, v224
	v_cvt_pk_bf16_f32 v85, v225, v226
	v_cvt_pk_bf16_f32 v86, v227, v228
	v_cvt_pk_bf16_f32 v87, v229, v230
	v_cvt_pk_bf16_f32 v88, v201, v202
	v_cvt_pk_bf16_f32 v89, v203, v204
	v_cvt_pk_bf16_f32 v90, v205, v206
	v_cvt_pk_bf16_f32 v91, v207, v231
	v_cvt_pk_bf16_f32 v92, v232, v233
	v_cvt_pk_bf16_f32 v93, v234, v235
	v_cvt_pk_bf16_f32 v94, v236, v237
	v_cvt_pk_bf16_f32 v95, v238, v95
	s_cmp_gt_u32 s55, 32
	s_cbranch_scc1 .LBB0_794
	s_cmp_lt_u32 s55, 29
	s_cselect_b32 s0, 0, 0xffffffe0
	s_cselect_b32 s1, s18, s16
	s_add_i32 s0, s0, s28
	s_lshl_b32 s0, s0, 6
	s_add_i32 s0, s0, s1
	s_mul_i32 s64, s0, 0x1800
	s_add_u32 s66, s78, s64
	s_addc_u32 s67, s79, 0
	s_add_u32 s68, s66, 0x30000
	s_addc_u32 s69, s67, 0
	s_add_u32 s70, s80, s64
	s_addc_u32 s71, s81, 0
	s_add_u32 s72, s70, 0x30000
	s_addc_u32 s73, s71, 0
	global_load_dwordx4 v[130:133], v241, s[66:67]
	global_load_dwordx4 v[134:137], v241, s[68:69]
	global_load_dwordx4 v[138:141], v241, s[70:71]
	global_load_dwordx4 v[142:145], v241, s[72:73]

.LBB0_795:
	s_add_i32 s20, s20, 0
	v_add_u32_e32 v80, s20, v184
	s_waitcnt vmcnt(4)
	s_waitcnt vmcnt(3)
	ds_write_b128 v80, v[146:149] offset:1024
	s_waitcnt vmcnt(2)
	ds_write_b128 v80, v[150:153] offset:9216
	v_add_u32_e32 v80, s20, v182
	s_waitcnt vmcnt(1)
	ds_write_b128 v80, v[154:157] offset:50176
	v_cmp_gt_f32_e32 vcc, 1.0, v197
	s_waitcnt vmcnt(0)
	ds_write_b128 v80, v[158:161] offset:58368
	s_cbranch_vccz .LBB0_799
	s_and_saveexec_b64 s[0:1], s[38:39]
	ds_write_b32 v178, v197 offset:128
	s_or_b64 exec, exec, s[0:1]
	s_waitcnt lgkmcnt(0)
	v_add_u32_e32 v92, v177, v112
	ds_read_b128 v[80:83], v92 offset:224
	ds_read_b128 v[84:87], v92 offset:192
	ds_read_b128 v[88:91], v92 offset:160
	ds_read_b128 v[92:95], v92 offset:128
	s_waitcnt lgkmcnt(3)
	v_pk_mul_f32 v[12:13], v[12:13], v[80:81]
	s_waitcnt lgkmcnt(2)
	v_pk_mul_f32 v[8:9], v[8:9], v[84:85]
	s_waitcnt lgkmcnt(1)
	v_pk_mul_f32 v[4:5], v[4:5], v[88:89]
	v_pk_mul_f32 v[14:15], v[14:15], v[82:83]
	v_pk_mul_f32 v[10:11], v[10:11], v[86:87]
	v_pk_mul_f32 v[6:7], v[6:7], v[90:91]
	s_waitcnt lgkmcnt(0)
	v_pk_mul_f32 v[2:3], v[2:3], v[94:95]
	v_pk_mul_f32 v[0:1], v[0:1], v[92:93]
	v_pk_mul_f32 v[60:61], v[60:61], v[80:81]
	v_pk_mul_f32 v[56:57], v[56:57], v[84:85]
	v_pk_mul_f32 v[52:53], v[52:53], v[88:89]
	v_pk_mul_f32 v[62:63], v[62:63], v[82:83]
	v_pk_mul_f32 v[58:59], v[58:59], v[86:87]
	v_pk_mul_f32 v[54:55], v[54:55], v[90:91]
	v_pk_mul_f32 v[50:51], v[50:51], v[94:95]
	v_pk_mul_f32 v[48:49], v[48:49], v[92:93]
	v_pk_mul_f32 v[44:45], v[44:45], v[80:81]
	v_pk_mul_f32 v[40:41], v[40:41], v[84:85]
	v_pk_mul_f32 v[36:37], v[36:37], v[88:89]
	v_pk_mul_f32 v[46:47], v[46:47], v[82:83]
	v_pk_mul_f32 v[42:43], v[42:43], v[86:87]
	v_pk_mul_f32 v[38:39], v[38:39], v[90:91]
	v_pk_mul_f32 v[34:35], v[34:35], v[94:95]
	v_pk_mul_f32 v[32:33], v[32:33], v[92:93]
	v_pk_mul_f32 v[28:29], v[28:29], v[80:81]
	v_pk_mul_f32 v[24:25], v[24:25], v[84:85]
	v_pk_mul_f32 v[20:21], v[20:21], v[88:89]
	v_pk_mul_f32 v[30:31], v[30:31], v[82:83]
	v_pk_mul_f32 v[26:27], v[26:27], v[86:87]
	v_pk_mul_f32 v[22:23], v[22:23], v[90:91]
	v_pk_mul_f32 v[18:19], v[18:19], v[94:95]
	v_pk_mul_f32 v[16:17], v[16:17], v[92:93]
